# ml_out: entering-state copy global->LDS unrolled, 9 loads in flight with counted waits (was a 9-trip load/vmcnt(0)/ds_write loop); on top of v49
# speedup vs baseline: 1.0160x; 1.0006x over previous
.LBB0_683:
	s_or_b64 exec, exec, s[56:57]
	s_waitcnt vmcnt(0)
	v_cndmask_b32_e64 v8, 0, 1, s[12:13]
	v_cmp_ne_u32_e64 s[56:57], 1, v8
	s_andn2_b64 vcc, exec, s[12:13]
	s_mov_b32 s45, 1
	s_cbranch_vccnz .LBB0_687
	s_mul_i32 s12, s46, 0x11000
	v_readlane_b32 s13, v254, 15
	s_add_u32 s12, s13, s12
	v_readlane_b32 s13, v254, 16
	s_addc_u32 s13, s13, 0
	s_mov_b64 s[58:59], 0
	v_mov_b32_e32 v8, v0
	v_mov_b32_e32 v8, v0
	v_mul_u32_u24_e32 v9, 0xf0f1, v8
	v_lshrrev_b32_e32 v9, 21, v9
	v_mul_u32_u24_e32 v14, 34, v9
	v_sub_u32_e32 v14, v8, v14
	v_mul_u32_u24_e32 v10, 0x220, v9
	v_lshl_add_u32 v10, v14, 4, v10
	v_mul_u32_u24_e32 v9, 0x230, v9
	v_lshl_add_u32 v136, v14, 4, v9
	global_load_dwordx4 v[100:103], v10, s[12:13]
	v_add_u32_e32 v8, 0x200, v0
	v_mul_u32_u24_e32 v9, 0xf0f1, v8
	v_lshrrev_b32_e32 v9, 21, v9
	v_mul_u32_u24_e32 v14, 34, v9
	v_sub_u32_e32 v14, v8, v14
	v_mul_u32_u24_e32 v10, 0x220, v9
	v_lshl_add_u32 v10, v14, 4, v10
	v_mul_u32_u24_e32 v9, 0x230, v9
	v_lshl_add_u32 v137, v14, 4, v9
	global_load_dwordx4 v[104:107], v10, s[12:13]
	v_add_u32_e32 v8, 0x400, v0
	v_mul_u32_u24_e32 v9, 0xf0f1, v8
	v_lshrrev_b32_e32 v9, 21, v9
	v_mul_u32_u24_e32 v14, 34, v9
	v_sub_u32_e32 v14, v8, v14
	v_mul_u32_u24_e32 v10, 0x220, v9
	v_lshl_add_u32 v10, v14, 4, v10
	v_mul_u32_u24_e32 v9, 0x230, v9
	v_lshl_add_u32 v138, v14, 4, v9
	global_load_dwordx4 v[108:111], v10, s[12:13]
	v_add_u32_e32 v8, 0x600, v0
	v_mul_u32_u24_e32 v9, 0xf0f1, v8
	v_lshrrev_b32_e32 v9, 21, v9
	v_mul_u32_u24_e32 v14, 34, v9
	v_sub_u32_e32 v14, v8, v14
	v_mul_u32_u24_e32 v10, 0x220, v9
	v_lshl_add_u32 v10, v14, 4, v10
	v_mul_u32_u24_e32 v9, 0x230, v9
	v_lshl_add_u32 v139, v14, 4, v9
	global_load_dwordx4 v[112:115], v10, s[12:13]
	v_add_u32_e32 v8, 0x800, v0
	v_mul_u32_u24_e32 v9, 0xf0f1, v8
	v_lshrrev_b32_e32 v9, 21, v9
	v_mul_u32_u24_e32 v14, 34, v9
	v_sub_u32_e32 v14, v8, v14
	v_mul_u32_u24_e32 v10, 0x220, v9
	v_lshl_add_u32 v10, v14, 4, v10
	v_mul_u32_u24_e32 v9, 0x230, v9
	v_lshl_add_u32 v140, v14, 4, v9
	global_load_dwordx4 v[116:119], v10, s[12:13]
	v_add_u32_e32 v8, 0xa00, v0
	v_mul_u32_u24_e32 v9, 0xf0f1, v8
	v_lshrrev_b32_e32 v9, 21, v9
	v_mul_u32_u24_e32 v14, 34, v9
	v_sub_u32_e32 v14, v8, v14
	v_mul_u32_u24_e32 v10, 0x220, v9
	v_lshl_add_u32 v10, v14, 4, v10
	v_mul_u32_u24_e32 v9, 0x230, v9
	v_lshl_add_u32 v141, v14, 4, v9
	global_load_dwordx4 v[120:123], v10, s[12:13]
	v_add_u32_e32 v8, 0xc00, v0
	v_mul_u32_u24_e32 v9, 0xf0f1, v8
	v_lshrrev_b32_e32 v9, 21, v9
	v_mul_u32_u24_e32 v14, 34, v9
	v_sub_u32_e32 v14, v8, v14
	v_mul_u32_u24_e32 v10, 0x220, v9
	v_lshl_add_u32 v10, v14, 4, v10
	v_mul_u32_u24_e32 v9, 0x230, v9
	v_lshl_add_u32 v142, v14, 4, v9
	global_load_dwordx4 v[124:127], v10, s[12:13]
	v_add_u32_e32 v8, 0xe00, v0
	v_mul_u32_u24_e32 v9, 0xf0f1, v8
	v_lshrrev_b32_e32 v9, 21, v9
	v_mul_u32_u24_e32 v14, 34, v9
	v_sub_u32_e32 v14, v8, v14
	v_mul_u32_u24_e32 v10, 0x220, v9
	v_lshl_add_u32 v10, v14, 4, v10
	v_mul_u32_u24_e32 v9, 0x230, v9
	v_lshl_add_u32 v143, v14, 4, v9
	global_load_dwordx4 v[128:131], v10, s[12:13]
	v_cmp_gt_u32_e32 vcc, 0x100, v0
	s_and_saveexec_b64 s[58:59], vcc
	v_add_u32_e32 v8, 0x1000, v0
	v_mul_u32_u24_e32 v9, 0xf0f1, v8
	v_lshrrev_b32_e32 v9, 21, v9
	v_mul_u32_u24_e32 v14, 34, v9
	v_sub_u32_e32 v14, v8, v14
	v_mul_u32_u24_e32 v10, 0x220, v9
	v_lshl_add_u32 v10, v14, 4, v10
	v_mul_u32_u24_e32 v9, 0x230, v9
	v_lshl_add_u32 v144, v14, 4, v9
	global_load_dwordx4 v[132:135], v10, s[12:13]
	s_or_b64 exec, exec, s[58:59]
	s_waitcnt vmcnt(8)
	ds_write_b128 v136, v[100:103]
	s_waitcnt vmcnt(7)
	ds_write_b128 v137, v[104:107]
	s_waitcnt vmcnt(6)
	ds_write_b128 v138, v[108:111]
	s_waitcnt vmcnt(5)
	ds_write_b128 v139, v[112:115]
	s_waitcnt vmcnt(4)
	ds_write_b128 v140, v[116:119]
	s_waitcnt vmcnt(3)
	ds_write_b128 v141, v[120:123]
	s_waitcnt vmcnt(2)
	ds_write_b128 v142, v[124:127]
	s_waitcnt vmcnt(1)
	ds_write_b128 v143, v[128:131]
	s_waitcnt vmcnt(0)
	s_and_saveexec_b64 s[58:59], vcc
	ds_write_b128 v144, v[132:135]
	s_or_b64 exec, exec, s[58:59]
	s_mov_b32 s45, 2
